# expert-conversion batch of the attention phase is assigned statically (batch = workgroup id: 256 batches, 256 workgroups) instead of a device-atomic claim
# baseline (speedup 1.0000x reference)
; #define LAS __attribute__((address_space(3)))
; __device__ __forceinline__ void attn_conv_batches(LAS unsigned char* lds, int wv, int l, int max_batches) {
;     ...
;         { volatile LAS int* slot = (volatile LAS int*)(lds + MISC_OFF + 512);
;           if (F.tid == 0) *slot = (int)__hip_atomic_fetch_add(cq, 1u, __ATOMIC_RELAXED, __HIP_MEMORY_SCOPE_AGENT);
;           __syncthreads(); bt = *slot; __syncthreads(); }
;         if (bt >= 3 * 2048 / 24) break;
;     ...
;     if (conv_now) attn_conv_batches(lds, wv, l, 1);
.LBB0_896:
	s_andn2_b64 vcc, exec, s[14:15]
	s_cbranch_vccnz .LBB0_913
	s_mov_b64 s[2:3], s[24:25]
	s_load_dwordx2 s[14:15], s[2:3], 0xf0
	s_mov_b32 s1, -1
	s_mov_b64 s[2:3], s[24:25]
	s_load_dwordx4 s[40:43], s[2:3], 0xc0
	s_load_dwordx2 s[16:17], s[2:3], 0xd0
	v_mbcnt_lo_u32_b32 v0, s1, 0
	v_mbcnt_hi_u32_b32 v2, s1, v0
	s_lshl_b32 s10, s72, 4
	v_readlane_b32 s1, v253, 8
	s_ashr_i32 s11, s10, 31
	s_nop 0
	v_cmp_eq_u32_e32 vcc, s1, v2
	s_and_saveexec_b64 s[34:35], vcc
	s_cbranch_execz .LBB0_901
	s_mov_b64 s[54:55], exec
	v_mbcnt_lo_u32_b32 v0, s54, 0
	v_mbcnt_hi_u32_b32 v0, s55, v0
	v_cmp_eq_u32_e32 vcc, 0, v0
	s_and_saveexec_b64 s[44:45], vcc
	s_cbranch_execz .LBB0_900
	s_lshl_b64 s[2:3], s[10:11], 2
	s_waitcnt lgkmcnt(0)
	s_add_u32 s2, s14, s2
	s_addc_u32 s3, s15, s3
	s_bcnt1_i32_b64 s1, s[54:55]
	v_mov_b32_e32 v1, s1
	v_mov_b32_e32 v1, s92
	s_nop 0

; #define LAS __attribute__((address_space(3)))
; __device__ __forceinline__ void attn_conv_batches(LAS unsigned char* lds, int wv, int l, int max_batches) {
;     ...
;         { volatile LAS int* slot = (volatile LAS int*)(lds + MISC_OFF + 512);
;           if (F.tid == 0) *slot = (int)__hip_atomic_fetch_add(cq, 1u, __ATOMIC_RELAXED, __HIP_MEMORY_SCOPE_AGENT);
;           __syncthreads(); bt = *slot; __syncthreads(); }
;         if (bt >= 3 * 2048 / 24) break;
;     ...
;     if (qs == 0 && l + 1 < L && !conv_now) attn_conv_batches(lds, wv, l, 1);
.LBB0_975:
	s_cmp_gt_i32 s72, 2
	s_cselect_b64 s[10:11], -1, 0
	s_or_b64 s[10:11], s[10:11], s[48:49]
	s_and_b64 vcc, exec, s[10:11]
	s_cbranch_vccnz .LBB0_992
	s_mov_b64 s[10:11], s[24:25]
	s_mov_b32 s3, -1
	s_mov_b64 s[14:15], s[24:25]
	s_load_dwordx2 s[10:11], s[10:11], 0xf0
	s_load_dwordx4 s[40:43], s[14:15], 0xc0
	s_nop 0
	s_load_dwordx2 s[14:15], s[14:15], 0xd0
	v_mbcnt_lo_u32_b32 v0, s3, 0
	v_mbcnt_hi_u32_b32 v2, s3, v0
	v_readlane_b32 s3, v253, 8
	s_nop 1
	v_cmp_eq_u32_e32 vcc, s3, v2
	s_and_saveexec_b64 s[16:17], vcc
	s_cbranch_execz .LBB0_980
	s_mov_b64 s[44:45], exec
	v_mbcnt_lo_u32_b32 v0, s44, 0
	v_mbcnt_hi_u32_b32 v0, s45, v0
	v_cmp_eq_u32_e32 vcc, 0, v0
	s_and_saveexec_b64 s[34:35], vcc
	s_cbranch_execz .LBB0_979
	v_readlane_b32 s20, v255, 7
	v_readlane_b32 s21, v255, 8
	s_waitcnt lgkmcnt(0)
	s_add_u32 s20, s10, s20
	s_addc_u32 s21, s11, s21
	s_bcnt1_i32_b64 s3, s[44:45]
	v_mov_b32_e32 v1, s3
	v_mov_b32_e32 v1, s92
	s_nop 0
